# P2: softmax denominator accumulated with f32 VALU adds (half-wave partials joined after the key loop) instead of two ones-operand MFMAs per key tile: 8 MFMAs per tile instead of 10
# speedup vs baseline: 1.0061x; 1.0061x over previous
.LBB0_323:
	s_ashr_i32 s7, s7, 2
	s_and_b64 s[8:9], s[86:87], exec
	s_cselect_b32 s57, 0, s7
	s_add_i32 s7, s22, s3
	s_add_i32 s8, s7, -4
	s_cmp_gt_i32 s7, 4
	s_cselect_b32 s8, s8, 0
	v_mov_b32_e32 v81, 0
	s_cmp_gt_i32 s8, s7
	s_cbranch_scc1 .LBB0_337
	s_max_i32 s70, s7, 4
	s_lshl_b32 s29, s57, 7
	s_lshl_b32 s30, s70, 5
	s_add_i32 s8, s30, s29
	v_add_u32_e32 v3, s8, v204
	v_mad_u64_u32 v[192:193], s[8:9], v3, s38, v[186:187]
	s_add_i32 s8, s63, s29
	s_mov_b32 s26, s12
	s_mov_b32 s27, s12
	s_add_i32 s8, s8, s30
	v_mov_b32_e32 v16, v2
	v_mov_b32_e32 v17, v2
	s_mov_b32 s13, s12
	s_mov_b32 s14, s12
	s_mov_b32 s15, s12
	s_mov_b32 s16, s12
	s_mov_b32 s17, s12
	s_mov_b32 s18, s12
	s_mov_b32 s19, s12
	s_mov_b32 s20, s12
	s_mov_b32 s21, s12
	s_mov_b32 s22, s12
	s_mov_b32 s23, s12
	s_mov_b32 s24, s12
	s_mov_b32 s25, s12
	s_lshl_b32 s8, s8, 7
	v_mov_b32_e32 v3, v2
	v_mov_b32_e32 v4, v2
	v_mov_b32_e32 v5, v2
	v_mov_b32_e32 v6, v2
	v_mov_b32_e32 v7, v2
	v_mov_b32_e32 v8, v2
	v_mov_b32_e32 v9, v2
	v_mov_b32_e32 v10, v2
	v_mov_b32_e32 v11, v2
	v_mov_b32_e32 v12, v2
	v_mov_b32_e32 v13, v2
	v_mov_b32_e32 v14, v2
	v_mov_b32_e32 v15, v2
	v_mov_b64_e32 v[64:65], s[26:27]
	v_mov_b64_e32 v[80:81], v[16:17]
	v_mov_b64_e32 v[96:97], v[16:17]
	s_add_i32 s69, s7, 4
	v_add_u32_e32 v193, s8, v202
	v_add_u32_e32 v206, s8, v203
	v_mov_b64_e32 v[62:63], s[24:25]
	v_mov_b64_e32 v[60:61], s[22:23]
	v_mov_b64_e32 v[58:59], s[20:21]
	v_mov_b64_e32 v[56:57], s[18:19]
	v_mov_b64_e32 v[54:55], s[16:17]
	v_mov_b64_e32 v[52:53], s[14:15]
	v_mov_b64_e32 v[50:51], s[12:13]
	v_mul_f32_e32 v50, 0.5, v50
	v_mov_b64_e32 v[78:79], v[14:15]
	v_mov_b64_e32 v[76:77], v[12:13]
	v_mov_b64_e32 v[74:75], v[10:11]
	v_mov_b64_e32 v[72:73], v[8:9]
	v_mov_b64_e32 v[70:71], v[6:7]
	v_mov_b64_e32 v[68:69], v[4:5]
	v_mov_b64_e32 v[66:67], v[2:3]
	v_mov_b64_e32 v[94:95], v[14:15]
	v_mov_b64_e32 v[92:93], v[12:13]
	v_mov_b64_e32 v[90:91], v[10:11]
	v_mov_b64_e32 v[88:89], v[8:9]
	v_mov_b64_e32 v[86:87], v[6:7]
	v_mov_b64_e32 v[84:85], v[4:5]
	v_mov_b64_e32 v[82:83], v[2:3]
	v_add_u32_e32 v3, 0, v192
	ds_read_b128 v[178:181], v3
	ds_read_b128 v[174:177], v3 offset:16
	ds_read_b128 v[170:173], v3 offset:32
	ds_read_b128 v[166:169], v3 offset:48

.LBB0_335:
	v_sub_f32_e32 v3, v98, v205
	v_sub_f32_e32 v98, v101, v205
	v_sub_f32_e32 v16, v99, v205
	v_exp_f32_e32 v99, v98
	v_sub_f32_e32 v98, v102, v205
	v_sub_f32_e32 v17, v100, v205
	v_exp_f32_e32 v100, v98
	v_sub_f32_e32 v98, v103, v205
	v_exp_f32_e32 v101, v98
	v_sub_f32_e32 v98, v104, v205
	v_exp_f32_e32 v102, v98
	v_sub_f32_e32 v98, v105, v205
	v_exp_f32_e32 v103, v98
	v_sub_f32_e32 v98, v106, v205
	v_exp_f32_e32 v104, v98
	v_sub_f32_e32 v98, v107, v205
	v_exp_f32_e32 v105, v98
	v_sub_f32_e32 v98, v108, v205
	v_exp_f32_e32 v106, v98
	v_sub_f32_e32 v98, v109, v205
	v_exp_f32_e32 v3, v3
	v_exp_f32_e32 v16, v16
	v_exp_f32_e32 v17, v17
	v_exp_f32_e32 v107, v98
	v_sub_f32_e32 v98, v110, v205
	v_exp_f32_e32 v108, v98
	v_sub_f32_e32 v98, v111, v205
	v_exp_f32_e32 v109, v98
	v_sub_f32_e32 v98, v112, v205
	v_exp_f32_e32 v110, v98
	v_sub_f32_e32 v98, v113, v205
	v_exp_f32_e32 v111, v98
	v_add_f32_e32 v244, v3, v16
	v_add_f32_e32 v245, v17, v99
	v_pk_add_f32 v[246:247], v[100:101], v[102:103]
	v_pk_add_f32 v[244:245], v[244:245], v[104:105]
	v_pk_add_f32 v[246:247], v[246:247], v[106:107]
	v_pk_add_f32 v[244:245], v[244:245], v[108:109]
	v_pk_add_f32 v[246:247], v[246:247], v[110:111]
	v_pk_add_f32 v[244:245], v[244:245], v[246:247]
	v_add_f32_e32 v244, v244, v245
	v_add_f32_e32 v50, v50, v244
	v_cvt_pk_bf16_f32 v98, v3, v16
	v_cvt_pk_bf16_f32 v99, v17, v99
	v_cvt_pk_bf16_f32 v100, v100, v101
	v_cvt_pk_bf16_f32 v101, v102, v103
	s_waitcnt lgkmcnt(2)
	v_mfma_f32_32x32x16_bf16 v[82:97], v[12:15], v[98:101], v[82:97]
	v_cvt_pk_bf16_f32 v102, v104, v105
	v_cvt_pk_bf16_f32 v103, v106, v107
	v_cvt_pk_bf16_f32 v104, v108, v109
	v_cvt_pk_bf16_f32 v105, v110, v111
	v_mfma_f32_32x32x16_bf16 v[66:81], v[162:165], v[98:101], v[66:81]
	s_add_i32 s8, s70, 1
	s_add_i32 s9, s70, -4
	v_add_u32_e32 v192, 0x1200, v192
	v_add_u32_e32 v193, 0x1000, v193
	v_add_u32_e32 v206, 0x1000, v206
	s_cmp_ge_i32 s9, s7
	v_mfma_f32_32x32x16_bf16 v[66:81], v[4:7], v[102:105], v[66:81]
	s_waitcnt lgkmcnt(0)
	v_mfma_f32_32x32x16_bf16 v[82:97], v[8:11], v[102:105], v[82:97]
	s_cbranch_scc1 .Lp2_lsum
	s_mov_b32 s70, s8
	s_branch .LBB0_325
.Lp2_lsum:
	v_mov_b32_e32 v244, v50
	s_nop 1
	v_permlane32_swap_b32_e32 v244, v50
	v_add_f32_e32 v50, v244, v50
	s_branch .LBB0_338
